# out-projection epilogue: accumulators lane-transposed (16x4 -> 4x16 via ds_bpermute) so each quad of lanes loads/stores one cache line instead of four; deep prefetch kept
# baseline (speedup 1.0000x reference)
; __device__ __forceinline__ unsigned cvt_pk_bf16(float lo, float hi) { unsigned r; asm volatile("v_cvt_pk_bf16_f32 %0, %1, %2" : "=v"(r) : "v"(lo), "v"(hi)); return r; }
;     __device__ __forceinline__ void operator()(const f32x4 (&acc)[2][2][4][2], const pg8::Unit& u, int wr, int wc, int fr, int fq) const {
;         const int row0 = u.pm * 256 + wr * 64 + fr, col0 = u.pn * 256 + wc * 32 + 8 * fq, b = (u.pm * 256) / S;
;         f32x4 gv[2][2];
; #pragma unroll
;         for (int bj = 0; bj < 2; ++bj)
; #pragma unroll
;             for (int n = 0; n < 2; ++n) gv[bj][n] = *(const f32x4*)(gm + (size_t)b * 6144 + col0 + bj * 128 + n * 4);
;     ...
;         constexpr int PF = 4;
;         if (xin32) {
;             f32x4 xq[PF][2];
; #pragma unroll
;             for (int it = 0; it < PF; ++it) { xq[it][0] = __builtin_nontemporal_load((const f32x4*)(xin32 + EO_OFF(it))); xq[it][1] = __builtin_nontemporal_load((const f32x4*)(xin32 + EO_OFF(it) + 4)); }
; #pragma unroll
;             for (int it = 0; it < 16; ++it) {
;                 const int ai = it >> 3, m = (it >> 1) & 3, bj = it & 1;
;                 const f32x4 x0 = xq[it % PF][0], x1 = xq[it % PF][1];
;                 if (it + PF < 16) { xq[it % PF][0] = __builtin_nontemporal_load((const f32x4*)(xin32 + EO_OFF(it + PF))); xq[it % PF][1] = __builtin_nontemporal_load((const f32x4*)(xin32 + EO_OFF(it + PF) + 4)); }
;                 const f32x4 v0 = x0 + gv[bj][0] * acc[ai][bj][m][0], v1 = x1 + gv[bj][1] * acc[ai][bj][m][1];
;                 u32x4 w; w.x = pg8::cvt_pk_bf16(v0[0], v0[1]); w.y = pg8::cvt_pk_bf16(v0[2], v0[3]); w.z = pg8::cvt_pk_bf16(v1[0], v1[1]); w.w = pg8::cvt_pk_bf16(v1[2], v1[3]);
;                 *(u32x4*)(out + EO_OFF(it)) = w;
;             }
.LBB0_720:
	s_ashr_i32 s15, s43, 31
	s_lshr_b32 s15, s15, 28
	s_add_i32 s15, s43, s15
	s_ashr_i32 s15, s15, 4
	s_mul_hi_i32 s17, s15, 0x6000
	s_mulk_i32 s15, 0x6000
	v_and_b32_e32 v232, 63, v0
	v_and_b32_e32 v233, 3, v232
	v_lshrrev_b32_e32 v234, 2, v232
	v_and_b32_e32 v235, 15, v232
	v_lshrrev_b32_e32 v232, 4, v232
	v_sub_u32_e32 v244, v234, v235
	v_sub_u32_e32 v245, v233, v232
	v_add_u32_e32 v246, v1, v244
	v_lshl_add_u32 v247, v245, 3, v248
	v_lshl_add_u32 v233, v233, 4, v234
	v_lshl_or_b32 v204, s44, 8, v247
	s_add_u32 s22, s36, s15
	s_addc_u32 s23, s37, s17
	v_lshlrev_b32_e32 v205, 2, v204
	s_lshl_b32 s15, s43, 19
	global_load_dwordx4 v[60:63], v205, s[22:23] offset:16
	global_load_dwordx4 v[64:67], v205, s[22:23]
	global_load_dwordx4 v[52:55], v205, s[22:23] offset:528
	global_load_dwordx4 v[56:59], v205, s[22:23] offset:512
	s_add_u32 s26, s50, s15
	s_addc_u32 s27, s51, 0
	v_lshlrev_b32_e32 v207, 1, v204
	v_lshl_add_u32 v206, v246, 12, v205
	v_lshl_add_u32 v207, v246, 11, v207
	v_lshlrev_b32_e32 v204, 2, v233
	s_andn2_b64 vcc, exec, s[12:13]
	s_cbranch_vccnz .Lop_epi_bf16
	s_lshl_b32 s15, s43, 20
	s_add_u32 s24, s8, s15
	s_addc_u32 s25, s9, 0
	ds_bpermute_b32 v144, v204, v144
	ds_bpermute_b32 v145, v204, v145
	ds_bpermute_b32 v146, v204, v146
	ds_bpermute_b32 v147, v204, v147
	ds_bpermute_b32 v140, v204, v140
	ds_bpermute_b32 v141, v204, v141
	ds_bpermute_b32 v142, v204, v142
	ds_bpermute_b32 v143, v204, v143
	s_add_u32 s28, s24, 0x0
	s_addc_u32 s29, s25, 0
	global_load_dwordx4 v[148:151], v206, s[28:29] nt
	global_load_dwordx4 v[152:155], v206, s[28:29] offset:16 nt
	global_load_dwordx4 v[156:159], v206, s[28:29] offset:512 nt
	global_load_dwordx4 v[160:163], v206, s[28:29] offset:528 nt
	s_add_u32 s28, s24, 0x10000
	s_addc_u32 s29, s25, 0
	global_load_dwordx4 v[164:167], v206, s[28:29] nt
	global_load_dwordx4 v[168:171], v206, s[28:29] offset:16 nt
	global_load_dwordx4 v[172:175], v206, s[28:29] offset:512 nt
	global_load_dwordx4 v[176:179], v206, s[28:29] offset:528 nt
	s_add_u32 s28, s24, 0x20000
	s_addc_u32 s29, s25, 0
	global_load_dwordx4 v[180:183], v206, s[28:29] nt
	global_load_dwordx4 v[184:187], v206, s[28:29] offset:16 nt
	global_load_dwordx4 v[208:211], v206, s[28:29] offset:512 nt
	global_load_dwordx4 v[212:215], v206, s[28:29] offset:528 nt
	s_add_u32 s28, s24, 0x30000
	s_addc_u32 s29, s25, 0
	global_load_dwordx4 v[216:219], v206, s[28:29] nt
	global_load_dwordx4 v[220:223], v206, s[28:29] offset:16 nt
	global_load_dwordx4 v[224:227], v206, s[28:29] offset:512 nt
	global_load_dwordx4 v[228:231], v206, s[28:29] offset:528 nt
	s_add_u32 s32, s26, 0x0
	s_addc_u32 s33, s27, 0
	s_add_u32 s28, s24, 0x80000
	s_addc_u32 s29, s25, 0
	s_waitcnt lgkmcnt(0)
	ds_bpermute_b32 v136, v204, v136
	ds_bpermute_b32 v137, v204, v137
	ds_bpermute_b32 v138, v204, v138
	ds_bpermute_b32 v139, v204, v139
	ds_bpermute_b32 v132, v204, v132
	ds_bpermute_b32 v133, v204, v133
	ds_bpermute_b32 v134, v204, v134
	ds_bpermute_b32 v135, v204, v135
	s_waitcnt vmcnt(14)
	v_pk_fma_f32 v[148:149], v[144:145], v[64:65], v[148:149]
	v_pk_fma_f32 v[150:151], v[146:147], v[66:67], v[150:151]
	v_pk_fma_f32 v[152:153], v[140:141], v[60:61], v[152:153]
	v_pk_fma_f32 v[154:155], v[142:143], v[62:63], v[154:155]
	v_cvt_pk_bf16_f32 v148, v148, v149
	v_cvt_pk_bf16_f32 v149, v150, v151
	v_cvt_pk_bf16_f32 v150, v152, v153
	v_cvt_pk_bf16_f32 v151, v154, v155
	global_store_dwordx4 v207, v[148:151], s[32:33]
	global_load_dwordx4 v[148:151], v206, s[28:29] nt
	global_load_dwordx4 v[152:155], v206, s[28:29] offset:16 nt
	s_waitcnt lgkmcnt(0)
	ds_bpermute_b32 v128, v204, v128
	ds_bpermute_b32 v129, v204, v129
	ds_bpermute_b32 v130, v204, v130
	ds_bpermute_b32 v131, v204, v131
	ds_bpermute_b32 v124, v204, v124
	ds_bpermute_b32 v125, v204, v125
	ds_bpermute_b32 v126, v204, v126
	ds_bpermute_b32 v127, v204, v127
	s_waitcnt vmcnt(15)
	v_pk_fma_f32 v[156:157], v[136:137], v[56:57], v[156:157]
	v_pk_fma_f32 v[158:159], v[138:139], v[58:59], v[158:159]
	v_pk_fma_f32 v[160:161], v[132:133], v[52:53], v[160:161]
	v_pk_fma_f32 v[162:163], v[134:135], v[54:55], v[162:163]
	v_cvt_pk_bf16_f32 v156, v156, v157
	v_cvt_pk_bf16_f32 v157, v158, v159
	v_cvt_pk_bf16_f32 v158, v160, v161
	v_cvt_pk_bf16_f32 v159, v162, v163
	global_store_dwordx4 v207, v[156:159], s[32:33] offset:256
	global_load_dwordx4 v[156:159], v206, s[28:29] offset:512 nt
	global_load_dwordx4 v[160:163], v206, s[28:29] offset:528 nt
	s_add_u32 s32, s26, 0x8000
	s_addc_u32 s33, s27, 0
	s_add_u32 s28, s24, 0x90000
	s_addc_u32 s29, s25, 0
	s_waitcnt lgkmcnt(0)
	ds_bpermute_b32 v120, v204, v120
	ds_bpermute_b32 v121, v204, v121
	ds_bpermute_b32 v122, v204, v122
	ds_bpermute_b32 v123, v204, v123
	ds_bpermute_b32 v116, v204, v116
	ds_bpermute_b32 v117, v204, v117
	ds_bpermute_b32 v118, v204, v118
	ds_bpermute_b32 v119, v204, v119
	s_waitcnt vmcnt(16)
	v_pk_fma_f32 v[164:165], v[128:129], v[64:65], v[164:165]
	v_pk_fma_f32 v[166:167], v[130:131], v[66:67], v[166:167]
	v_pk_fma_f32 v[168:169], v[124:125], v[60:61], v[168:169]
	v_pk_fma_f32 v[170:171], v[126:127], v[62:63], v[170:171]
	v_cvt_pk_bf16_f32 v164, v164, v165
	v_cvt_pk_bf16_f32 v165, v166, v167
	v_cvt_pk_bf16_f32 v166, v168, v169
	v_cvt_pk_bf16_f32 v167, v170, v171
	global_store_dwordx4 v207, v[164:167], s[32:33]
	global_load_dwordx4 v[164:167], v206, s[28:29] nt
	global_load_dwordx4 v[168:171], v206, s[28:29] offset:16 nt
	s_waitcnt lgkmcnt(0)
	ds_bpermute_b32 v112, v204, v112
	ds_bpermute_b32 v113, v204, v113
	ds_bpermute_b32 v114, v204, v114
	ds_bpermute_b32 v115, v204, v115
	ds_bpermute_b32 v108, v204, v108
	ds_bpermute_b32 v109, v204, v109
	ds_bpermute_b32 v110, v204, v110
	ds_bpermute_b32 v111, v204, v111
	s_waitcnt vmcnt(17)
; __device__ __forceinline__ unsigned cvt_pk_bf16(float lo, float hi) { unsigned r; asm volatile("v_cvt_pk_bf16_f32 %0, %1, %2" : "=v"(r) : "v"(lo), "v"(hi)); return r; }
;     __device__ __forceinline__ void operator()(const f32x4 (&acc)[2][2][4][2], const pg8::Unit& u, int wr, int wc, int fr, int fq) const {
;     ...
;             for (int it = 0; it < 16; ++it) {
;                 const int ai = it >> 3, m = (it >> 1) & 3, bj = it & 1;
;                 const f32x4 x0 = xq[it % PF][0], x1 = xq[it % PF][1];
;                 if (it + PF < 16) { xq[it % PF][0] = __builtin_nontemporal_load((const f32x4*)(xin32 + EO_OFF(it + PF))); xq[it % PF][1] = __builtin_nontemporal_load((const f32x4*)(xin32 + EO_OFF(it + PF) + 4)); }
;                 const f32x4 v0 = x0 + gv[bj][0] * acc[ai][bj][m][0], v1 = x1 + gv[bj][1] * acc[ai][bj][m][1];
;                 u32x4 w; w.x = pg8::cvt_pk_bf16(v0[0], v0[1]); w.y = pg8::cvt_pk_bf16(v0[2], v0[3]); w.z = pg8::cvt_pk_bf16(v1[0], v1[1]); w.w = pg8::cvt_pk_bf16(v1[2], v1[3]);
;                 *(u32x4*)(out + EO_OFF(it)) = w;
;             }
	v_pk_fma_f32 v[172:173], v[120:121], v[56:57], v[172:173]
	v_pk_fma_f32 v[174:175], v[122:123], v[58:59], v[174:175]
	v_pk_fma_f32 v[176:177], v[116:117], v[52:53], v[176:177]
	v_pk_fma_f32 v[178:179], v[118:119], v[54:55], v[178:179]
	v_cvt_pk_bf16_f32 v172, v172, v173
	v_cvt_pk_bf16_f32 v173, v174, v175
	v_cvt_pk_bf16_f32 v174, v176, v177
	v_cvt_pk_bf16_f32 v175, v178, v179
	global_store_dwordx4 v207, v[172:175], s[32:33] offset:256
	global_load_dwordx4 v[172:175], v206, s[28:29] offset:512 nt
	global_load_dwordx4 v[176:179], v206, s[28:29] offset:528 nt
	s_add_u32 s32, s26, 0x10000
	s_addc_u32 s33, s27, 0
	s_add_u32 s28, s24, 0xa0000
	s_addc_u32 s29, s25, 0
	s_waitcnt lgkmcnt(0)
	ds_bpermute_b32 v104, v204, v104
	ds_bpermute_b32 v105, v204, v105
	ds_bpermute_b32 v106, v204, v106
	ds_bpermute_b32 v107, v204, v107
	ds_bpermute_b32 v100, v204, v100
	ds_bpermute_b32 v101, v204, v101
	ds_bpermute_b32 v102, v204, v102
	ds_bpermute_b32 v103, v204, v103
	s_waitcnt vmcnt(18)
	v_pk_fma_f32 v[180:181], v[112:113], v[64:65], v[180:181]
	v_pk_fma_f32 v[182:183], v[114:115], v[66:67], v[182:183]
	v_pk_fma_f32 v[184:185], v[108:109], v[60:61], v[184:185]
	v_pk_fma_f32 v[186:187], v[110:111], v[62:63], v[186:187]
	v_cvt_pk_bf16_f32 v180, v180, v181
	v_cvt_pk_bf16_f32 v181, v182, v183
	v_cvt_pk_bf16_f32 v182, v184, v185
	v_cvt_pk_bf16_f32 v183, v186, v187
	global_store_dwordx4 v207, v[180:183], s[32:33]
	global_load_dwordx4 v[180:183], v206, s[28:29] nt
	global_load_dwordx4 v[184:187], v206, s[28:29] offset:16 nt
	s_waitcnt lgkmcnt(0)
	ds_bpermute_b32 v96, v204, v96
	ds_bpermute_b32 v97, v204, v97
	ds_bpermute_b32 v98, v204, v98
	ds_bpermute_b32 v99, v204, v99
	ds_bpermute_b32 v92, v204, v92
	ds_bpermute_b32 v93, v204, v93
	ds_bpermute_b32 v94, v204, v94
	ds_bpermute_b32 v95, v204, v95
	s_waitcnt vmcnt(19)
	v_pk_fma_f32 v[208:209], v[104:105], v[56:57], v[208:209]
	v_pk_fma_f32 v[210:211], v[106:107], v[58:59], v[210:211]
	v_pk_fma_f32 v[212:213], v[100:101], v[52:53], v[212:213]
	v_pk_fma_f32 v[214:215], v[102:103], v[54:55], v[214:215]
	v_cvt_pk_bf16_f32 v208, v208, v209
	v_cvt_pk_bf16_f32 v209, v210, v211
	v_cvt_pk_bf16_f32 v210, v212, v213
	v_cvt_pk_bf16_f32 v211, v214, v215
	global_store_dwordx4 v207, v[208:211], s[32:33] offset:256
	global_load_dwordx4 v[208:211], v206, s[28:29] offset:512 nt
	global_load_dwordx4 v[212:215], v206, s[28:29] offset:528 nt
	s_add_u32 s32, s26, 0x18000
	s_addc_u32 s33, s27, 0
	s_add_u32 s28, s24, 0xb0000
	s_addc_u32 s29, s25, 0
	s_waitcnt lgkmcnt(0)
	ds_bpermute_b32 v88, v204, v88
	ds_bpermute_b32 v89, v204, v89
	ds_bpermute_b32 v90, v204, v90
	ds_bpermute_b32 v91, v204, v91
	ds_bpermute_b32 v84, v204, v84
	ds_bpermute_b32 v85, v204, v85
	ds_bpermute_b32 v86, v204, v86
	ds_bpermute_b32 v87, v204, v87
	s_waitcnt vmcnt(20)
	v_pk_fma_f32 v[216:217], v[96:97], v[64:65], v[216:217]
	v_pk_fma_f32 v[218:219], v[98:99], v[66:67], v[218:219]
	v_pk_fma_f32 v[220:221], v[92:93], v[60:61], v[220:221]
	v_pk_fma_f32 v[222:223], v[94:95], v[62:63], v[222:223]
	v_cvt_pk_bf16_f32 v216, v216, v217
	v_cvt_pk_bf16_f32 v217, v218, v219
	v_cvt_pk_bf16_f32 v218, v220, v221
	v_cvt_pk_bf16_f32 v219, v222, v223
	global_store_dwordx4 v207, v[216:219], s[32:33]
	global_load_dwordx4 v[216:219], v206, s[28:29] nt
	global_load_dwordx4 v[220:223], v206, s[28:29] offset:16 nt
	s_waitcnt lgkmcnt(0)
	ds_bpermute_b32 v80, v204, v80
	ds_bpermute_b32 v81, v204, v81
	ds_bpermute_b32 v82, v204, v82
	ds_bpermute_b32 v83, v204, v83
	ds_bpermute_b32 v76, v204, v76
	ds_bpermute_b32 v77, v204, v77
	ds_bpermute_b32 v78, v204, v78
	ds_bpermute_b32 v79, v204, v79
	s_waitcnt vmcnt(21)
	v_pk_fma_f32 v[224:225], v[88:89], v[56:57], v[224:225]
	v_pk_fma_f32 v[226:227], v[90:91], v[58:59], v[226:227]
	v_pk_fma_f32 v[228:229], v[84:85], v[52:53], v[228:229]
	v_pk_fma_f32 v[230:231], v[86:87], v[54:55], v[230:231]
	v_cvt_pk_bf16_f32 v224, v224, v225
	v_cvt_pk_bf16_f32 v225, v226, v227
	v_cvt_pk_bf16_f32 v226, v228, v229
	v_cvt_pk_bf16_f32 v227, v230, v231
	global_store_dwordx4 v207, v[224:227], s[32:33] offset:256
	global_load_dwordx4 v[224:227], v206, s[28:29] offset:512 nt
	global_load_dwordx4 v[228:231], v206, s[28:29] offset:528 nt
	s_add_u32 s32, s26, 0x40000
	s_addc_u32 s33, s27, 0
	s_waitcnt lgkmcnt(0)
	ds_bpermute_b32 v72, v204, v72
	ds_bpermute_b32 v73, v204, v73
	ds_bpermute_b32 v74, v204, v74
	ds_bpermute_b32 v75, v204, v75
	ds_bpermute_b32 v68, v204, v68
	ds_bpermute_b32 v69, v204, v69
	ds_bpermute_b32 v70, v204, v70
	ds_bpermute_b32 v71, v204, v71
	s_waitcnt vmcnt(21)
	v_pk_fma_f32 v[148:149], v[80:81], v[64:65], v[148:149]
	v_pk_fma_f32 v[150:151], v[82:83], v[66:67], v[150:151]
	v_pk_fma_f32 v[152:153], v[76:77], v[60:61], v[152:153]
	v_pk_fma_f32 v[154:155], v[78:79], v[62:63], v[154:155]
	v_cvt_pk_bf16_f32 v148, v148, v149
	v_cvt_pk_bf16_f32 v149, v150, v151
	v_cvt_pk_bf16_f32 v150, v152, v153
	v_cvt_pk_bf16_f32 v151, v154, v155
	global_store_dwordx4 v207, v[148:151], s[32:33]
	s_waitcnt lgkmcnt(0)
	ds_bpermute_b32 v48, v204, v48
	ds_bpermute_b32 v49, v204, v49
	ds_bpermute_b32 v50, v204, v50
	ds_bpermute_b32 v51, v204, v51
	ds_bpermute_b32 v44, v204, v44
	ds_bpermute_b32 v45, v204, v45
	ds_bpermute_b32 v46, v204, v46
	ds_bpermute_b32 v47, v204, v47
	s_waitcnt vmcnt(19)
	v_pk_fma_f32 v[156:157], v[72:73], v[56:57], v[156:157]
	v_pk_fma_f32 v[158:159], v[74:75], v[58:59], v[158:159]
	v_pk_fma_f32 v[160:161], v[68:69], v[52:53], v[160:161]
	v_pk_fma_f32 v[162:163], v[70:71], v[54:55], v[162:163]
	v_cvt_pk_bf16_f32 v156, v156, v157
	v_cvt_pk_bf16_f32 v157, v158, v159
	v_cvt_pk_bf16_f32 v158, v160, v161
	v_cvt_pk_bf16_f32 v159, v162, v163
	global_store_dwordx4 v207, v[156:159], s[32:33] offset:256
	s_add_u32 s32, s26, 0x48000
	s_addc_u32 s33, s27, 0
	s_waitcnt lgkmcnt(0)
; __device__ __forceinline__ unsigned cvt_pk_bf16(float lo, float hi) { unsigned r; asm volatile("v_cvt_pk_bf16_f32 %0, %1, %2" : "=v"(r) : "v"(lo), "v"(hi)); return r; }
;     __device__ __forceinline__ void operator()(const f32x4 (&acc)[2][2][4][2], const pg8::Unit& u, int wr, int wc, int fr, int fq) const {
;     ...
;             for (int it = 0; it < 16; ++it) {
;                 const int ai = it >> 3, m = (it >> 1) & 3, bj = it & 1;
;                 const f32x4 x0 = xq[it % PF][0], x1 = xq[it % PF][1];
;                 if (it + PF < 16) { xq[it % PF][0] = __builtin_nontemporal_load((const f32x4*)(xin32 + EO_OFF(it + PF))); xq[it % PF][1] = __builtin_nontemporal_load((const f32x4*)(xin32 + EO_OFF(it + PF) + 4)); }
;                 const f32x4 v0 = x0 + gv[bj][0] * acc[ai][bj][m][0], v1 = x1 + gv[bj][1] * acc[ai][bj][m][1];
;                 u32x4 w; w.x = pg8::cvt_pk_bf16(v0[0], v0[1]); w.y = pg8::cvt_pk_bf16(v0[2], v0[3]); w.z = pg8::cvt_pk_bf16(v1[0], v1[1]); w.w = pg8::cvt_pk_bf16(v1[2], v1[3]);
;                 *(u32x4*)(out + EO_OFF(it)) = w;
;             }
;         } else {
;             u32x4 xq[PF];
; #pragma unroll
;             for (int it = 0; it < PF; ++it) xq[it] = __builtin_nontemporal_load((const u32x4*)(xin16 + EO_OFF(it)));
; #pragma unroll
;             for (int it = 0; it < 16; ++it) {
;                 const int ai = it >> 3, m = (it >> 1) & 3, bj = it & 1;
;                 const u32x4 xv = xq[it % PF];
;                 if (it + PF < 16) xq[it % PF] = __builtin_nontemporal_load((const u32x4*)(xin16 + EO_OFF(it + PF)));
;                 const f32x4 x0 = (f32x4){__uint_as_float(xv.x << 16), __uint_as_float(xv.x & 0xffff0000u), __uint_as_float(xv.y << 16), __uint_as_float(xv.y & 0xffff0000u)};
;                 const f32x4 x1 = (f32x4){__uint_as_float(xv.z << 16), __uint_as_float(xv.z & 0xffff0000u), __uint_as_float(xv.w << 16), __uint_as_float(xv.w & 0xffff0000u)};
;                 const f32x4 v0 = x0 + gv[bj][0] * acc[ai][bj][m][0], v1 = x1 + gv[bj][1] * acc[ai][bj][m][1];
;                 u32x4 w; w.x = pg8::cvt_pk_bf16(v0[0], v0[1]); w.y = pg8::cvt_pk_bf16(v0[2], v0[3]); w.z = pg8::cvt_pk_bf16(v1[0], v1[1]); w.w = pg8::cvt_pk_bf16(v1[2], v1[3]);
;                 *(u32x4*)(out + EO_OFF(it)) = w;
;             }
	ds_bpermute_b32 v40, v204, v40
	ds_bpermute_b32 v41, v204, v41
	ds_bpermute_b32 v42, v204, v42
	ds_bpermute_b32 v43, v204, v43
	ds_bpermute_b32 v36, v204, v36
	ds_bpermute_b32 v37, v204, v37
	ds_bpermute_b32 v38, v204, v38
	ds_bpermute_b32 v39, v204, v39
	s_waitcnt vmcnt(17)
	v_pk_fma_f32 v[164:165], v[48:49], v[64:65], v[164:165]
	v_pk_fma_f32 v[166:167], v[50:51], v[66:67], v[166:167]
	v_pk_fma_f32 v[168:169], v[44:45], v[60:61], v[168:169]
	v_pk_fma_f32 v[170:171], v[46:47], v[62:63], v[170:171]
	v_cvt_pk_bf16_f32 v164, v164, v165
	v_cvt_pk_bf16_f32 v165, v166, v167
	v_cvt_pk_bf16_f32 v166, v168, v169
	v_cvt_pk_bf16_f32 v167, v170, v171
	global_store_dwordx4 v207, v[164:167], s[32:33]
	s_waitcnt lgkmcnt(0)
	ds_bpermute_b32 v30, v204, v30
	ds_bpermute_b32 v31, v204, v31
	ds_bpermute_b32 v32, v204, v32
	ds_bpermute_b32 v33, v204, v33
	ds_bpermute_b32 v26, v204, v26
	ds_bpermute_b32 v27, v204, v27
	ds_bpermute_b32 v28, v204, v28
	ds_bpermute_b32 v29, v204, v29
	s_waitcnt vmcnt(15)
	v_pk_fma_f32 v[172:173], v[40:41], v[56:57], v[172:173]
	v_pk_fma_f32 v[174:175], v[42:43], v[58:59], v[174:175]
	v_pk_fma_f32 v[176:177], v[36:37], v[52:53], v[176:177]
	v_pk_fma_f32 v[178:179], v[38:39], v[54:55], v[178:179]
	v_cvt_pk_bf16_f32 v172, v172, v173
	v_cvt_pk_bf16_f32 v173, v174, v175
	v_cvt_pk_bf16_f32 v174, v176, v177
	v_cvt_pk_bf16_f32 v175, v178, v179
	global_store_dwordx4 v207, v[172:175], s[32:33] offset:256
	s_add_u32 s32, s26, 0x50000
	s_addc_u32 s33, s27, 0
	s_waitcnt lgkmcnt(0)
	ds_bpermute_b32 v22, v204, v22
	ds_bpermute_b32 v23, v204, v23
	ds_bpermute_b32 v24, v204, v24
	ds_bpermute_b32 v25, v204, v25
	ds_bpermute_b32 v18, v204, v18
	ds_bpermute_b32 v19, v204, v19
	ds_bpermute_b32 v20, v204, v20
	ds_bpermute_b32 v21, v204, v21
	s_waitcnt vmcnt(13)
	v_pk_fma_f32 v[180:181], v[30:31], v[64:65], v[180:181]
	v_pk_fma_f32 v[182:183], v[32:33], v[66:67], v[182:183]
	v_pk_fma_f32 v[184:185], v[26:27], v[60:61], v[184:185]
	v_pk_fma_f32 v[186:187], v[28:29], v[62:63], v[186:187]
	v_cvt_pk_bf16_f32 v180, v180, v181
	v_cvt_pk_bf16_f32 v181, v182, v183
	v_cvt_pk_bf16_f32 v182, v184, v185
	v_cvt_pk_bf16_f32 v183, v186, v187
	global_store_dwordx4 v207, v[180:183], s[32:33]
	s_waitcnt lgkmcnt(0)
	ds_bpermute_b32 v14, v204, v14
	ds_bpermute_b32 v15, v204, v15
	ds_bpermute_b32 v16, v204, v16
	ds_bpermute_b32 v17, v204, v17
	ds_bpermute_b32 v10, v204, v10
	ds_bpermute_b32 v11, v204, v11
	ds_bpermute_b32 v12, v204, v12
	ds_bpermute_b32 v13, v204, v13
	s_waitcnt vmcnt(11)
	v_pk_fma_f32 v[208:209], v[22:23], v[56:57], v[208:209]
	v_pk_fma_f32 v[210:211], v[24:25], v[58:59], v[210:211]
	v_pk_fma_f32 v[212:213], v[18:19], v[52:53], v[212:213]
	v_pk_fma_f32 v[214:215], v[20:21], v[54:55], v[214:215]
	v_cvt_pk_bf16_f32 v208, v208, v209
	v_cvt_pk_bf16_f32 v209, v210, v211
	v_cvt_pk_bf16_f32 v210, v212, v213
	v_cvt_pk_bf16_f32 v211, v214, v215
	global_store_dwordx4 v207, v[208:211], s[32:33] offset:256
	s_add_u32 s32, s26, 0x58000
	s_addc_u32 s33, s27, 0
	s_waitcnt lgkmcnt(0)
	ds_bpermute_b32 v6, v204, v6
	ds_bpermute_b32 v7, v204, v7
	ds_bpermute_b32 v8, v204, v8
	ds_bpermute_b32 v9, v204, v9
	ds_bpermute_b32 v2, v204, v2
	ds_bpermute_b32 v3, v204, v3
	ds_bpermute_b32 v4, v204, v4
	ds_bpermute_b32 v5, v204, v5
	s_waitcnt vmcnt(9)
	v_pk_fma_f32 v[216:217], v[14:15], v[64:65], v[216:217]
	v_pk_fma_f32 v[218:219], v[16:17], v[66:67], v[218:219]
	v_pk_fma_f32 v[220:221], v[10:11], v[60:61], v[220:221]
	v_pk_fma_f32 v[222:223], v[12:13], v[62:63], v[222:223]
	v_cvt_pk_bf16_f32 v216, v216, v217
	v_cvt_pk_bf16_f32 v217, v218, v219
	v_cvt_pk_bf16_f32 v218, v220, v221
	v_cvt_pk_bf16_f32 v219, v222, v223
	global_store_dwordx4 v207, v[216:219], s[32:33]
	s_waitcnt lgkmcnt(0)
	s_waitcnt vmcnt(7)
	v_pk_fma_f32 v[224:225], v[6:7], v[56:57], v[224:225]
	v_pk_fma_f32 v[226:227], v[8:9], v[58:59], v[226:227]
	v_pk_fma_f32 v[228:229], v[2:3], v[52:53], v[228:229]
	v_pk_fma_f32 v[230:231], v[4:5], v[54:55], v[230:231]
	v_cvt_pk_bf16_f32 v224, v224, v225
	v_cvt_pk_bf16_f32 v225, v226, v227
	v_cvt_pk_bf16_f32 v226, v228, v229
	v_cvt_pk_bf16_f32 v227, v230, v231
	global_store_dwordx4 v207, v[224:227], s[32:33] offset:256
	s_branch .Lop_epi_done
.Lop_epi_bf16:
	ds_bpermute_b32 v144, v204, v144
	ds_bpermute_b32 v145, v204, v145
	ds_bpermute_b32 v146, v204, v146
	ds_bpermute_b32 v147, v204, v147
	ds_bpermute_b32 v140, v204, v140
	ds_bpermute_b32 v141, v204, v141
	ds_bpermute_b32 v142, v204, v142
	ds_bpermute_b32 v143, v204, v143
	s_add_u32 s28, s26, 0x0
	s_addc_u32 s29, s27, 0
	global_load_dwordx4 v[148:151], v207, s[28:29] nt
	global_load_dwordx4 v[152:155], v207, s[28:29] offset:256 nt
	s_add_u32 s28, s26, 0x8000
	s_addc_u32 s29, s27, 0
	global_load_dwordx4 v[156:159], v207, s[28:29] nt
	global_load_dwordx4 v[160:163], v207, s[28:29] offset:256 nt
	s_add_u32 s28, s26, 0x10000
	s_addc_u32 s29, s27, 0
	global_load_dwordx4 v[164:167], v207, s[28:29] nt
	global_load_dwordx4 v[168:171], v207, s[28:29] offset:256 nt
	s_add_u32 s28, s26, 0x18000
	s_addc_u32 s29, s27, 0
	global_load_dwordx4 v[172:175], v207, s[28:29] nt
	global_load_dwordx4 v[176:179], v207, s[28:29] offset:256 nt
	s_add_u32 s28, s26, 0x40000
	s_addc_u32 s29, s27, 0
	global_load_dwordx4 v[180:183], v207, s[28:29] nt
	global_load_dwordx4 v[184:187], v207, s[28:29] offset:256 nt
	s_add_u32 s28, s26, 0x48000
	s_addc_u32 s29, s27, 0
	global_load_dwordx4 v[208:211], v207, s[28:29] nt
	global_load_dwordx4 v[212:215], v207, s[28:29] offset:256 nt
	s_add_u32 s28, s26, 0x50000
	s_addc_u32 s29, s27, 0
	global_load_dwordx4 v[216:219], v207, s[28:29] nt
	global_load_dwordx4 v[220:223], v207, s[28:29] offset:256 nt
	s_add_u32 s28, s26, 0x58000
	s_addc_u32 s29, s27, 0
	global_load_dwordx4 v[224:227], v207, s[28:29] nt
	global_load_dwordx4 v[228:231], v207, s[28:29] offset:256 nt
	s_add_u32 s32, s26, 0x0
	s_addc_u32 s33, s27, 0
	s_waitcnt lgkmcnt(0)
; __device__ __forceinline__ unsigned cvt_pk_bf16(float lo, float hi) { unsigned r; asm volatile("v_cvt_pk_bf16_f32 %0, %1, %2" : "=v"(r) : "v"(lo), "v"(hi)); return r; }
;     __device__ __forceinline__ void operator()(const f32x4 (&acc)[2][2][4][2], const pg8::Unit& u, int wr, int wc, int fr, int fq) const {
;     ...
;             for (int it = 0; it < 16; ++it) {
;                 const int ai = it >> 3, m = (it >> 1) & 3, bj = it & 1;
;                 const u32x4 xv = xq[it % PF];
;                 if (it + PF < 16) xq[it % PF] = __builtin_nontemporal_load((const u32x4*)(xin16 + EO_OFF(it + PF)));
;                 const f32x4 x0 = (f32x4){__uint_as_float(xv.x << 16), __uint_as_float(xv.x & 0xffff0000u), __uint_as_float(xv.y << 16), __uint_as_float(xv.y & 0xffff0000u)};
;                 const f32x4 x1 = (f32x4){__uint_as_float(xv.z << 16), __uint_as_float(xv.z & 0xffff0000u), __uint_as_float(xv.w << 16), __uint_as_float(xv.w & 0xffff0000u)};
;                 const f32x4 v0 = x0 + gv[bj][0] * acc[ai][bj][m][0], v1 = x1 + gv[bj][1] * acc[ai][bj][m][1];
;                 u32x4 w; w.x = pg8::cvt_pk_bf16(v0[0], v0[1]); w.y = pg8::cvt_pk_bf16(v0[2], v0[3]); w.z = pg8::cvt_pk_bf16(v1[0], v1[1]); w.w = pg8::cvt_pk_bf16(v1[2], v1[3]);
;                 *(u32x4*)(out + EO_OFF(it)) = w;
;             }
	ds_bpermute_b32 v136, v204, v136
	ds_bpermute_b32 v137, v204, v137
	ds_bpermute_b32 v138, v204, v138
	ds_bpermute_b32 v139, v204, v139
	ds_bpermute_b32 v132, v204, v132
	ds_bpermute_b32 v133, v204, v133
	ds_bpermute_b32 v134, v204, v134
	ds_bpermute_b32 v135, v204, v135
	s_waitcnt vmcnt(15)
	v_lshlrev_b32_e32 v232, 16, v148
	v_and_b32_e32 v233, 0xffff0000, v148
	v_lshlrev_b32_e32 v234, 16, v149
	v_and_b32_e32 v235, 0xffff0000, v149
	v_lshlrev_b32_e32 v244, 16, v150
	v_and_b32_e32 v245, 0xffff0000, v150
	v_lshlrev_b32_e32 v246, 16, v151
	v_and_b32_e32 v247, 0xffff0000, v151
	v_pk_fma_f32 v[144:145], v[144:145], v[64:65], v[232:233]
	v_pk_fma_f32 v[146:147], v[146:147], v[66:67], v[234:235]
	v_pk_fma_f32 v[140:141], v[140:141], v[60:61], v[244:245]
	v_pk_fma_f32 v[142:143], v[142:143], v[62:63], v[246:247]
	v_cvt_pk_bf16_f32 v148, v144, v145
	v_cvt_pk_bf16_f32 v149, v146, v147
	v_cvt_pk_bf16_f32 v150, v140, v141
	v_cvt_pk_bf16_f32 v151, v142, v143
	global_store_dwordx4 v207, v[148:151], s[32:33]
	s_waitcnt lgkmcnt(0)
	ds_bpermute_b32 v128, v204, v128
	ds_bpermute_b32 v129, v204, v129
	ds_bpermute_b32 v130, v204, v130
	ds_bpermute_b32 v131, v204, v131
	ds_bpermute_b32 v124, v204, v124
	ds_bpermute_b32 v125, v204, v125
	ds_bpermute_b32 v126, v204, v126
	ds_bpermute_b32 v127, v204, v127
	s_waitcnt vmcnt(15)
	v_lshlrev_b32_e32 v232, 16, v152
	v_and_b32_e32 v233, 0xffff0000, v152
	v_lshlrev_b32_e32 v234, 16, v153
	v_and_b32_e32 v235, 0xffff0000, v153
	v_lshlrev_b32_e32 v244, 16, v154
	v_and_b32_e32 v245, 0xffff0000, v154
	v_lshlrev_b32_e32 v246, 16, v155
	v_and_b32_e32 v247, 0xffff0000, v155
	v_pk_fma_f32 v[136:137], v[136:137], v[56:57], v[232:233]
	v_pk_fma_f32 v[138:139], v[138:139], v[58:59], v[234:235]
	v_pk_fma_f32 v[132:133], v[132:133], v[52:53], v[244:245]
	v_pk_fma_f32 v[134:135], v[134:135], v[54:55], v[246:247]
	v_cvt_pk_bf16_f32 v152, v136, v137
	v_cvt_pk_bf16_f32 v153, v138, v139
	v_cvt_pk_bf16_f32 v154, v132, v133
	v_cvt_pk_bf16_f32 v155, v134, v135
	global_store_dwordx4 v207, v[152:155], s[32:33] offset:256
	s_add_u32 s32, s26, 0x8000
	s_addc_u32 s33, s27, 0
	s_waitcnt lgkmcnt(0)
	ds_bpermute_b32 v120, v204, v120
	ds_bpermute_b32 v121, v204, v121
	ds_bpermute_b32 v122, v204, v122
	ds_bpermute_b32 v123, v204, v123
	ds_bpermute_b32 v116, v204, v116
	ds_bpermute_b32 v117, v204, v117
	ds_bpermute_b32 v118, v204, v118
	ds_bpermute_b32 v119, v204, v119
	s_waitcnt vmcnt(15)
	v_lshlrev_b32_e32 v232, 16, v156
	v_and_b32_e32 v233, 0xffff0000, v156
	v_lshlrev_b32_e32 v234, 16, v157
	v_and_b32_e32 v235, 0xffff0000, v157
	v_lshlrev_b32_e32 v244, 16, v158
	v_and_b32_e32 v245, 0xffff0000, v158
	v_lshlrev_b32_e32 v246, 16, v159
	v_and_b32_e32 v247, 0xffff0000, v159
	v_pk_fma_f32 v[128:129], v[128:129], v[64:65], v[232:233]
	v_pk_fma_f32 v[130:131], v[130:131], v[66:67], v[234:235]
	v_pk_fma_f32 v[124:125], v[124:125], v[60:61], v[244:245]
	v_pk_fma_f32 v[126:127], v[126:127], v[62:63], v[246:247]
	v_cvt_pk_bf16_f32 v156, v128, v129
	v_cvt_pk_bf16_f32 v157, v130, v131
	v_cvt_pk_bf16_f32 v158, v124, v125
	v_cvt_pk_bf16_f32 v159, v126, v127
	global_store_dwordx4 v207, v[156:159], s[32:33]
	s_waitcnt lgkmcnt(0)
	ds_bpermute_b32 v112, v204, v112
	ds_bpermute_b32 v113, v204, v113
	ds_bpermute_b32 v114, v204, v114
	ds_bpermute_b32 v115, v204, v115
	ds_bpermute_b32 v108, v204, v108
	ds_bpermute_b32 v109, v204, v109
	ds_bpermute_b32 v110, v204, v110
	ds_bpermute_b32 v111, v204, v111
	s_waitcnt vmcnt(15)
	v_lshlrev_b32_e32 v232, 16, v160
	v_and_b32_e32 v233, 0xffff0000, v160
	v_lshlrev_b32_e32 v234, 16, v161
	v_and_b32_e32 v235, 0xffff0000, v161
	v_lshlrev_b32_e32 v244, 16, v162
	v_and_b32_e32 v245, 0xffff0000, v162
	v_lshlrev_b32_e32 v246, 16, v163
	v_and_b32_e32 v247, 0xffff0000, v163
	v_pk_fma_f32 v[120:121], v[120:121], v[56:57], v[232:233]
	v_pk_fma_f32 v[122:123], v[122:123], v[58:59], v[234:235]
	v_pk_fma_f32 v[116:117], v[116:117], v[52:53], v[244:245]
	v_pk_fma_f32 v[118:119], v[118:119], v[54:55], v[246:247]
	v_cvt_pk_bf16_f32 v160, v120, v121
	v_cvt_pk_bf16_f32 v161, v122, v123
	v_cvt_pk_bf16_f32 v162, v116, v117
	v_cvt_pk_bf16_f32 v163, v118, v119
	global_store_dwordx4 v207, v[160:163], s[32:33] offset:256
	s_add_u32 s32, s26, 0x10000
	s_addc_u32 s33, s27, 0
	s_waitcnt lgkmcnt(0)
	ds_bpermute_b32 v104, v204, v104
	ds_bpermute_b32 v105, v204, v105
	ds_bpermute_b32 v106, v204, v106
	ds_bpermute_b32 v107, v204, v107
	ds_bpermute_b32 v100, v204, v100
	ds_bpermute_b32 v101, v204, v101
	ds_bpermute_b32 v102, v204, v102
	ds_bpermute_b32 v103, v204, v103
	s_waitcnt vmcnt(15)
	v_lshlrev_b32_e32 v232, 16, v164
	v_and_b32_e32 v233, 0xffff0000, v164
	v_lshlrev_b32_e32 v234, 16, v165
	v_and_b32_e32 v235, 0xffff0000, v165
	v_lshlrev_b32_e32 v244, 16, v166
	v_and_b32_e32 v245, 0xffff0000, v166
	v_lshlrev_b32_e32 v246, 16, v167
	v_and_b32_e32 v247, 0xffff0000, v167
	v_pk_fma_f32 v[112:113], v[112:113], v[64:65], v[232:233]
	v_pk_fma_f32 v[114:115], v[114:115], v[66:67], v[234:235]
	v_pk_fma_f32 v[108:109], v[108:109], v[60:61], v[244:245]
	v_pk_fma_f32 v[110:111], v[110:111], v[62:63], v[246:247]
	v_cvt_pk_bf16_f32 v164, v112, v113
	v_cvt_pk_bf16_f32 v165, v114, v115
	v_cvt_pk_bf16_f32 v166, v108, v109
	v_cvt_pk_bf16_f32 v167, v110, v111
	global_store_dwordx4 v207, v[164:167], s[32:33]
	s_waitcnt lgkmcnt(0)
	ds_bpermute_b32 v96, v204, v96
	ds_bpermute_b32 v97, v204, v97
	ds_bpermute_b32 v98, v204, v98
	ds_bpermute_b32 v99, v204, v99
	ds_bpermute_b32 v92, v204, v92
	ds_bpermute_b32 v93, v204, v93
	ds_bpermute_b32 v94, v204, v94
	ds_bpermute_b32 v95, v204, v95
	s_waitcnt vmcnt(15)
; __device__ __forceinline__ unsigned cvt_pk_bf16(float lo, float hi) { unsigned r; asm volatile("v_cvt_pk_bf16_f32 %0, %1, %2" : "=v"(r) : "v"(lo), "v"(hi)); return r; }
;     __device__ __forceinline__ void operator()(const f32x4 (&acc)[2][2][4][2], const pg8::Unit& u, int wr, int wc, int fr, int fq) const {
;     ...
;             for (int it = 0; it < 16; ++it) {
;                 const int ai = it >> 3, m = (it >> 1) & 3, bj = it & 1;
;                 const u32x4 xv = xq[it % PF];
;                 if (it + PF < 16) xq[it % PF] = __builtin_nontemporal_load((const u32x4*)(xin16 + EO_OFF(it + PF)));
;                 const f32x4 x0 = (f32x4){__uint_as_float(xv.x << 16), __uint_as_float(xv.x & 0xffff0000u), __uint_as_float(xv.y << 16), __uint_as_float(xv.y & 0xffff0000u)};
;                 const f32x4 x1 = (f32x4){__uint_as_float(xv.z << 16), __uint_as_float(xv.z & 0xffff0000u), __uint_as_float(xv.w << 16), __uint_as_float(xv.w & 0xffff0000u)};
;                 const f32x4 v0 = x0 + gv[bj][0] * acc[ai][bj][m][0], v1 = x1 + gv[bj][1] * acc[ai][bj][m][1];
;                 u32x4 w; w.x = pg8::cvt_pk_bf16(v0[0], v0[1]); w.y = pg8::cvt_pk_bf16(v0[2], v0[3]); w.z = pg8::cvt_pk_bf16(v1[0], v1[1]); w.w = pg8::cvt_pk_bf16(v1[2], v1[3]);
;                 *(u32x4*)(out + EO_OFF(it)) = w;
;             }
	v_lshlrev_b32_e32 v232, 16, v168
	v_and_b32_e32 v233, 0xffff0000, v168
	v_lshlrev_b32_e32 v234, 16, v169
	v_and_b32_e32 v235, 0xffff0000, v169
	v_lshlrev_b32_e32 v244, 16, v170
	v_and_b32_e32 v245, 0xffff0000, v170
	v_lshlrev_b32_e32 v246, 16, v171
	v_and_b32_e32 v247, 0xffff0000, v171
	v_pk_fma_f32 v[104:105], v[104:105], v[56:57], v[232:233]
	v_pk_fma_f32 v[106:107], v[106:107], v[58:59], v[234:235]
	v_pk_fma_f32 v[100:101], v[100:101], v[52:53], v[244:245]
	v_pk_fma_f32 v[102:103], v[102:103], v[54:55], v[246:247]
	v_cvt_pk_bf16_f32 v168, v104, v105
	v_cvt_pk_bf16_f32 v169, v106, v107
	v_cvt_pk_bf16_f32 v170, v100, v101
	v_cvt_pk_bf16_f32 v171, v102, v103
	global_store_dwordx4 v207, v[168:171], s[32:33] offset:256
	s_add_u32 s32, s26, 0x18000
	s_addc_u32 s33, s27, 0
	s_waitcnt lgkmcnt(0)
	ds_bpermute_b32 v88, v204, v88
	ds_bpermute_b32 v89, v204, v89
	ds_bpermute_b32 v90, v204, v90
	ds_bpermute_b32 v91, v204, v91
	ds_bpermute_b32 v84, v204, v84
	ds_bpermute_b32 v85, v204, v85
	ds_bpermute_b32 v86, v204, v86
	ds_bpermute_b32 v87, v204, v87
	s_waitcnt vmcnt(15)
	v_lshlrev_b32_e32 v232, 16, v172
	v_and_b32_e32 v233, 0xffff0000, v172
	v_lshlrev_b32_e32 v234, 16, v173
	v_and_b32_e32 v235, 0xffff0000, v173
	v_lshlrev_b32_e32 v244, 16, v174
	v_and_b32_e32 v245, 0xffff0000, v174
	v_lshlrev_b32_e32 v246, 16, v175
	v_and_b32_e32 v247, 0xffff0000, v175
	v_pk_fma_f32 v[96:97], v[96:97], v[64:65], v[232:233]
	v_pk_fma_f32 v[98:99], v[98:99], v[66:67], v[234:235]
	v_pk_fma_f32 v[92:93], v[92:93], v[60:61], v[244:245]
	v_pk_fma_f32 v[94:95], v[94:95], v[62:63], v[246:247]
	v_cvt_pk_bf16_f32 v172, v96, v97
	v_cvt_pk_bf16_f32 v173, v98, v99
	v_cvt_pk_bf16_f32 v174, v92, v93
	v_cvt_pk_bf16_f32 v175, v94, v95
	global_store_dwordx4 v207, v[172:175], s[32:33]
	s_waitcnt lgkmcnt(0)
	ds_bpermute_b32 v80, v204, v80
	ds_bpermute_b32 v81, v204, v81
	ds_bpermute_b32 v82, v204, v82
	ds_bpermute_b32 v83, v204, v83
	ds_bpermute_b32 v76, v204, v76
	ds_bpermute_b32 v77, v204, v77
	ds_bpermute_b32 v78, v204, v78
	ds_bpermute_b32 v79, v204, v79
	s_waitcnt vmcnt(15)
	v_lshlrev_b32_e32 v232, 16, v176
	v_and_b32_e32 v233, 0xffff0000, v176
	v_lshlrev_b32_e32 v234, 16, v177
	v_and_b32_e32 v235, 0xffff0000, v177
	v_lshlrev_b32_e32 v244, 16, v178
	v_and_b32_e32 v245, 0xffff0000, v178
	v_lshlrev_b32_e32 v246, 16, v179
	v_and_b32_e32 v247, 0xffff0000, v179
	v_pk_fma_f32 v[88:89], v[88:89], v[56:57], v[232:233]
	v_pk_fma_f32 v[90:91], v[90:91], v[58:59], v[234:235]
	v_pk_fma_f32 v[84:85], v[84:85], v[52:53], v[244:245]
	v_pk_fma_f32 v[86:87], v[86:87], v[54:55], v[246:247]
	v_cvt_pk_bf16_f32 v176, v88, v89
	v_cvt_pk_bf16_f32 v177, v90, v91
	v_cvt_pk_bf16_f32 v178, v84, v85
	v_cvt_pk_bf16_f32 v179, v86, v87
	global_store_dwordx4 v207, v[176:179], s[32:33] offset:256
	s_add_u32 s32, s26, 0x40000
	s_addc_u32 s33, s27, 0
	s_waitcnt lgkmcnt(0)
	ds_bpermute_b32 v72, v204, v72
	ds_bpermute_b32 v73, v204, v73
	ds_bpermute_b32 v74, v204, v74
	ds_bpermute_b32 v75, v204, v75
	ds_bpermute_b32 v68, v204, v68
	ds_bpermute_b32 v69, v204, v69
	ds_bpermute_b32 v70, v204, v70
	ds_bpermute_b32 v71, v204, v71
	s_waitcnt vmcnt(15)
	v_lshlrev_b32_e32 v232, 16, v180
	v_and_b32_e32 v233, 0xffff0000, v180
	v_lshlrev_b32_e32 v234, 16, v181
	v_and_b32_e32 v235, 0xffff0000, v181
	v_lshlrev_b32_e32 v244, 16, v182
	v_and_b32_e32 v245, 0xffff0000, v182
	v_lshlrev_b32_e32 v246, 16, v183
	v_and_b32_e32 v247, 0xffff0000, v183
	v_pk_fma_f32 v[80:81], v[80:81], v[64:65], v[232:233]
	v_pk_fma_f32 v[82:83], v[82:83], v[66:67], v[234:235]
	v_pk_fma_f32 v[76:77], v[76:77], v[60:61], v[244:245]
	v_pk_fma_f32 v[78:79], v[78:79], v[62:63], v[246:247]
	v_cvt_pk_bf16_f32 v180, v80, v81
	v_cvt_pk_bf16_f32 v181, v82, v83
	v_cvt_pk_bf16_f32 v182, v76, v77
	v_cvt_pk_bf16_f32 v183, v78, v79
	global_store_dwordx4 v207, v[180:183], s[32:33]
	s_waitcnt lgkmcnt(0)
	ds_bpermute_b32 v48, v204, v48
	ds_bpermute_b32 v49, v204, v49
	ds_bpermute_b32 v50, v204, v50
	ds_bpermute_b32 v51, v204, v51
	ds_bpermute_b32 v44, v204, v44
	ds_bpermute_b32 v45, v204, v45
	ds_bpermute_b32 v46, v204, v46
	ds_bpermute_b32 v47, v204, v47
	s_waitcnt vmcnt(15)
	v_lshlrev_b32_e32 v232, 16, v184
	v_and_b32_e32 v233, 0xffff0000, v184
	v_lshlrev_b32_e32 v234, 16, v185
	v_and_b32_e32 v235, 0xffff0000, v185
	v_lshlrev_b32_e32 v244, 16, v186
	v_and_b32_e32 v245, 0xffff0000, v186
	v_lshlrev_b32_e32 v246, 16, v187
	v_and_b32_e32 v247, 0xffff0000, v187
	v_pk_fma_f32 v[72:73], v[72:73], v[56:57], v[232:233]
	v_pk_fma_f32 v[74:75], v[74:75], v[58:59], v[234:235]
	v_pk_fma_f32 v[68:69], v[68:69], v[52:53], v[244:245]
	v_pk_fma_f32 v[70:71], v[70:71], v[54:55], v[246:247]
	v_cvt_pk_bf16_f32 v184, v72, v73
	v_cvt_pk_bf16_f32 v185, v74, v75
	v_cvt_pk_bf16_f32 v186, v68, v69
	v_cvt_pk_bf16_f32 v187, v70, v71
	global_store_dwordx4 v207, v[184:187], s[32:33] offset:256
	s_add_u32 s32, s26, 0x48000
	s_addc_u32 s33, s27, 0
	s_waitcnt lgkmcnt(0)
	ds_bpermute_b32 v40, v204, v40
	ds_bpermute_b32 v41, v204, v41
	ds_bpermute_b32 v42, v204, v42
	ds_bpermute_b32 v43, v204, v43
	ds_bpermute_b32 v36, v204, v36
	ds_bpermute_b32 v37, v204, v37
	ds_bpermute_b32 v38, v204, v38
	ds_bpermute_b32 v39, v204, v39
	s_waitcnt vmcnt(15)
; __device__ __forceinline__ unsigned cvt_pk_bf16(float lo, float hi) { unsigned r; asm volatile("v_cvt_pk_bf16_f32 %0, %1, %2" : "=v"(r) : "v"(lo), "v"(hi)); return r; }
;     __device__ __forceinline__ void operator()(const f32x4 (&acc)[2][2][4][2], const pg8::Unit& u, int wr, int wc, int fr, int fq) const {
;     ...
;             for (int it = 0; it < 16; ++it) {
;                 const int ai = it >> 3, m = (it >> 1) & 3, bj = it & 1;
;                 const u32x4 xv = xq[it % PF];
;                 if (it + PF < 16) xq[it % PF] = __builtin_nontemporal_load((const u32x4*)(xin16 + EO_OFF(it + PF)));
;                 const f32x4 x0 = (f32x4){__uint_as_float(xv.x << 16), __uint_as_float(xv.x & 0xffff0000u), __uint_as_float(xv.y << 16), __uint_as_float(xv.y & 0xffff0000u)};
;                 const f32x4 x1 = (f32x4){__uint_as_float(xv.z << 16), __uint_as_float(xv.z & 0xffff0000u), __uint_as_float(xv.w << 16), __uint_as_float(xv.w & 0xffff0000u)};
;                 const f32x4 v0 = x0 + gv[bj][0] * acc[ai][bj][m][0], v1 = x1 + gv[bj][1] * acc[ai][bj][m][1];
;                 u32x4 w; w.x = pg8::cvt_pk_bf16(v0[0], v0[1]); w.y = pg8::cvt_pk_bf16(v0[2], v0[3]); w.z = pg8::cvt_pk_bf16(v1[0], v1[1]); w.w = pg8::cvt_pk_bf16(v1[2], v1[3]);
;                 *(u32x4*)(out + EO_OFF(it)) = w;
;             }
	v_lshlrev_b32_e32 v232, 16, v208
	v_and_b32_e32 v233, 0xffff0000, v208
	v_lshlrev_b32_e32 v234, 16, v209
	v_and_b32_e32 v235, 0xffff0000, v209
	v_lshlrev_b32_e32 v244, 16, v210
	v_and_b32_e32 v245, 0xffff0000, v210
	v_lshlrev_b32_e32 v246, 16, v211
	v_and_b32_e32 v247, 0xffff0000, v211
	v_pk_fma_f32 v[48:49], v[48:49], v[64:65], v[232:233]
	v_pk_fma_f32 v[50:51], v[50:51], v[66:67], v[234:235]
	v_pk_fma_f32 v[44:45], v[44:45], v[60:61], v[244:245]
	v_pk_fma_f32 v[46:47], v[46:47], v[62:63], v[246:247]
	v_cvt_pk_bf16_f32 v208, v48, v49
	v_cvt_pk_bf16_f32 v209, v50, v51
	v_cvt_pk_bf16_f32 v210, v44, v45
	v_cvt_pk_bf16_f32 v211, v46, v47
	global_store_dwordx4 v207, v[208:211], s[32:33]
	s_waitcnt lgkmcnt(0)
	ds_bpermute_b32 v30, v204, v30
	ds_bpermute_b32 v31, v204, v31
	ds_bpermute_b32 v32, v204, v32
	ds_bpermute_b32 v33, v204, v33
	ds_bpermute_b32 v26, v204, v26
	ds_bpermute_b32 v27, v204, v27
	ds_bpermute_b32 v28, v204, v28
	ds_bpermute_b32 v29, v204, v29
	s_waitcnt vmcnt(15)
	v_lshlrev_b32_e32 v232, 16, v212
	v_and_b32_e32 v233, 0xffff0000, v212
	v_lshlrev_b32_e32 v234, 16, v213
	v_and_b32_e32 v235, 0xffff0000, v213
	v_lshlrev_b32_e32 v244, 16, v214
	v_and_b32_e32 v245, 0xffff0000, v214
	v_lshlrev_b32_e32 v246, 16, v215
	v_and_b32_e32 v247, 0xffff0000, v215
	v_pk_fma_f32 v[40:41], v[40:41], v[56:57], v[232:233]
	v_pk_fma_f32 v[42:43], v[42:43], v[58:59], v[234:235]
	v_pk_fma_f32 v[36:37], v[36:37], v[52:53], v[244:245]
	v_pk_fma_f32 v[38:39], v[38:39], v[54:55], v[246:247]
	v_cvt_pk_bf16_f32 v212, v40, v41
	v_cvt_pk_bf16_f32 v213, v42, v43
	v_cvt_pk_bf16_f32 v214, v36, v37
	v_cvt_pk_bf16_f32 v215, v38, v39
	global_store_dwordx4 v207, v[212:215], s[32:33] offset:256
	s_add_u32 s32, s26, 0x50000
	s_addc_u32 s33, s27, 0
	s_waitcnt lgkmcnt(0)
	ds_bpermute_b32 v22, v204, v22
	ds_bpermute_b32 v23, v204, v23
	ds_bpermute_b32 v24, v204, v24
	ds_bpermute_b32 v25, v204, v25
	ds_bpermute_b32 v18, v204, v18
	ds_bpermute_b32 v19, v204, v19
	ds_bpermute_b32 v20, v204, v20
	ds_bpermute_b32 v21, v204, v21
	s_waitcnt vmcnt(15)
	v_lshlrev_b32_e32 v232, 16, v216
	v_and_b32_e32 v233, 0xffff0000, v216
	v_lshlrev_b32_e32 v234, 16, v217
	v_and_b32_e32 v235, 0xffff0000, v217
	v_lshlrev_b32_e32 v244, 16, v218
	v_and_b32_e32 v245, 0xffff0000, v218
	v_lshlrev_b32_e32 v246, 16, v219
	v_and_b32_e32 v247, 0xffff0000, v219
	v_pk_fma_f32 v[30:31], v[30:31], v[64:65], v[232:233]
	v_pk_fma_f32 v[32:33], v[32:33], v[66:67], v[234:235]
	v_pk_fma_f32 v[26:27], v[26:27], v[60:61], v[244:245]
	v_pk_fma_f32 v[28:29], v[28:29], v[62:63], v[246:247]
	v_cvt_pk_bf16_f32 v216, v30, v31
	v_cvt_pk_bf16_f32 v217, v32, v33
	v_cvt_pk_bf16_f32 v218, v26, v27
	v_cvt_pk_bf16_f32 v219, v28, v29
	global_store_dwordx4 v207, v[216:219], s[32:33]
	s_waitcnt lgkmcnt(0)
	ds_bpermute_b32 v14, v204, v14
	ds_bpermute_b32 v15, v204, v15
	ds_bpermute_b32 v16, v204, v16
	ds_bpermute_b32 v17, v204, v17
	ds_bpermute_b32 v10, v204, v10
	ds_bpermute_b32 v11, v204, v11
	ds_bpermute_b32 v12, v204, v12
	ds_bpermute_b32 v13, v204, v13
	s_waitcnt vmcnt(15)
	v_lshlrev_b32_e32 v232, 16, v220
	v_and_b32_e32 v233, 0xffff0000, v220
	v_lshlrev_b32_e32 v234, 16, v221
	v_and_b32_e32 v235, 0xffff0000, v221
	v_lshlrev_b32_e32 v244, 16, v222
	v_and_b32_e32 v245, 0xffff0000, v222
	v_lshlrev_b32_e32 v246, 16, v223
	v_and_b32_e32 v247, 0xffff0000, v223
	v_pk_fma_f32 v[22:23], v[22:23], v[56:57], v[232:233]
	v_pk_fma_f32 v[24:25], v[24:25], v[58:59], v[234:235]
	v_pk_fma_f32 v[18:19], v[18:19], v[52:53], v[244:245]
	v_pk_fma_f32 v[20:21], v[20:21], v[54:55], v[246:247]
	v_cvt_pk_bf16_f32 v220, v22, v23
	v_cvt_pk_bf16_f32 v221, v24, v25
	v_cvt_pk_bf16_f32 v222, v18, v19
	v_cvt_pk_bf16_f32 v223, v20, v21
	global_store_dwordx4 v207, v[220:223], s[32:33] offset:256
	s_add_u32 s32, s26, 0x58000
	s_addc_u32 s33, s27, 0
	s_waitcnt lgkmcnt(0)
	ds_bpermute_b32 v6, v204, v6
	ds_bpermute_b32 v7, v204, v7
	ds_bpermute_b32 v8, v204, v8
	ds_bpermute_b32 v9, v204, v9
	ds_bpermute_b32 v2, v204, v2
	ds_bpermute_b32 v3, v204, v3
	ds_bpermute_b32 v4, v204, v4
	ds_bpermute_b32 v5, v204, v5
	s_waitcnt vmcnt(15)
	v_lshlrev_b32_e32 v232, 16, v224
	v_and_b32_e32 v233, 0xffff0000, v224
	v_lshlrev_b32_e32 v234, 16, v225
	v_and_b32_e32 v235, 0xffff0000, v225
	v_lshlrev_b32_e32 v244, 16, v226
	v_and_b32_e32 v245, 0xffff0000, v226
	v_lshlrev_b32_e32 v246, 16, v227
	v_and_b32_e32 v247, 0xffff0000, v227
	v_pk_fma_f32 v[14:15], v[14:15], v[64:65], v[232:233]
	v_pk_fma_f32 v[16:17], v[16:17], v[66:67], v[234:235]
	v_pk_fma_f32 v[10:11], v[10:11], v[60:61], v[244:245]
	v_pk_fma_f32 v[12:13], v[12:13], v[62:63], v[246:247]
	v_cvt_pk_bf16_f32 v224, v14, v15
	v_cvt_pk_bf16_f32 v225, v16, v17
	v_cvt_pk_bf16_f32 v226, v10, v11
	v_cvt_pk_bf16_f32 v227, v12, v13
	global_store_dwordx4 v207, v[224:227], s[32:33]
	s_waitcnt lgkmcnt(0)
	s_waitcnt vmcnt(15)
	v_lshlrev_b32_e32 v232, 16, v228
	v_and_b32_e32 v233, 0xffff0000, v228
	v_lshlrev_b32_e32 v234, 16, v229
	v_and_b32_e32 v235, 0xffff0000, v229
	v_lshlrev_b32_e32 v244, 16, v230
	v_and_b32_e32 v245, 0xffff0000, v230
	v_lshlrev_b32_e32 v246, 16, v231
	v_and_b32_e32 v247, 0xffff0000, v231
	v_pk_fma_f32 v[6:7], v[6:7], v[56:57], v[232:233]
	v_pk_fma_f32 v[8:9], v[8:9], v[58:59], v[234:235]
	v_pk_fma_f32 v[2:3], v[2:3], v[52:53], v[244:245]
	v_pk_fma_f32 v[4:5], v[4:5], v[54:55], v[246:247]
	v_cvt_pk_bf16_f32 v228, v6, v7
	v_cvt_pk_bf16_f32 v229, v8, v9
	v_cvt_pk_bf16_f32 v230, v2, v3
	v_cvt_pk_bf16_f32 v231, v4, v5
	global_store_dwordx4 v207, v[228:231], s[32:33] offset:256
